# hyena layer-1 hosting + phase-0 idle x prefetch + batched staging loads (filter W2, hyena staging, router matrix)
# speedup vs baseline: 1.0182x; 1.0063x over previous
; __device__ __forceinline__ void prologue0(Frame& F) {
;     for (int it = blockIdx.x; it < 192; it += F.G) mod_item(F, it);
; }
; __device__ __forceinline__ void prologue2(Frame& F) {
;     ...
;     for (int m = gw; m < M; m += NGW) { const int b = m >> 12; f32x4 v[4]; row_load(INP(F, I_X) + (size_t)m * DM, lane, v);
.Lp0_idle:
	v_mov_b32_e32 v3, 0x20000
	ds_read_b64 v[4:5], v3
	s_sub_u32 s2, s88, 0xc0
	s_lshl_b32 s2, s2, 3
	s_lshr_b32 s3, s14, 6
	s_add_u32 s2, s2, s3
	s_mul_i32 s2, s2, 98304
	v_lshlrev_b32_e32 v2, 6, v186
	s_waitcnt lgkmcnt(0)
	v_readfirstlane_b32 s0, v4
	v_readfirstlane_b32 s1, v5
	s_add_u32 s0, s0, s2
	s_addc_u32 s1, s1, 0
	global_load_dword v3, v2, s[0:1] nt
	s_add_u32 s0, s0, 0x1000
	s_addc_u32 s1, s1, 0
	global_load_dword v3, v2, s[0:1] nt
	s_add_u32 s0, s0, 0x1000
	s_addc_u32 s1, s1, 0
	global_load_dword v3, v2, s[0:1] nt
	s_add_u32 s0, s0, 0x1000
	s_addc_u32 s1, s1, 0
	global_load_dword v3, v2, s[0:1] nt
	s_add_u32 s0, s0, 0x1000
	s_addc_u32 s1, s1, 0
	global_load_dword v3, v2, s[0:1] nt
	s_add_u32 s0, s0, 0x1000
	s_addc_u32 s1, s1, 0
	global_load_dword v3, v2, s[0:1] nt
	s_add_u32 s0, s0, 0x1000
	s_addc_u32 s1, s1, 0
	global_load_dword v3, v2, s[0:1] nt
	s_add_u32 s0, s0, 0x1000
	s_addc_u32 s1, s1, 0
	global_load_dword v3, v2, s[0:1] nt
	s_add_u32 s0, s0, 0x1000
	s_addc_u32 s1, s1, 0
	global_load_dword v3, v2, s[0:1] nt
	s_add_u32 s0, s0, 0x1000
	s_addc_u32 s1, s1, 0
	global_load_dword v3, v2, s[0:1] nt
	s_add_u32 s0, s0, 0x1000
	s_addc_u32 s1, s1, 0
	global_load_dword v3, v2, s[0:1] nt
	s_add_u32 s0, s0, 0x1000
	s_addc_u32 s1, s1, 0
	global_load_dword v3, v2, s[0:1] nt
	s_add_u32 s0, s0, 0x1000
	s_addc_u32 s1, s1, 0
	global_load_dword v3, v2, s[0:1] nt
	s_add_u32 s0, s0, 0x1000
	s_addc_u32 s1, s1, 0
	global_load_dword v3, v2, s[0:1] nt
	s_add_u32 s0, s0, 0x1000
	s_addc_u32 s1, s1, 0
	global_load_dword v3, v2, s[0:1] nt
	s_add_u32 s0, s0, 0x1000
	s_addc_u32 s1, s1, 0
	global_load_dword v3, v2, s[0:1] nt
	s_add_u32 s0, s0, 0x1000
	s_addc_u32 s1, s1, 0
	global_load_dword v3, v2, s[0:1] nt
	s_add_u32 s0, s0, 0x1000
	s_addc_u32 s1, s1, 0
	global_load_dword v3, v2, s[0:1] nt
	s_add_u32 s0, s0, 0x1000
	s_addc_u32 s1, s1, 0
	global_load_dword v3, v2, s[0:1] nt
	s_add_u32 s0, s0, 0x1000
	s_addc_u32 s1, s1, 0
	global_load_dword v3, v2, s[0:1] nt
	s_add_u32 s0, s0, 0x1000
	s_addc_u32 s1, s1, 0
	global_load_dword v3, v2, s[0:1] nt
	s_add_u32 s0, s0, 0x1000
	s_addc_u32 s1, s1, 0
	global_load_dword v3, v2, s[0:1] nt
	s_add_u32 s0, s0, 0x1000
	s_addc_u32 s1, s1, 0
	global_load_dword v3, v2, s[0:1] nt
	s_add_u32 s0, s0, 0x1000
	s_addc_u32 s1, s1, 0
	global_load_dword v3, v2, s[0:1] nt
	s_add_u32 s0, s0, 0x1000
	s_addc_u32 s1, s1, 0

; __device__ __forceinline__ void filter_item(Frame& F, int it) {
;     ...
;     for (int i = tid; i < 2 * 64 * 64; i += NTHR) W2[i] = INP(F, I_HW2)[l * 2 * 64 * 64 + i];
.LBB0_83:
	s_waitcnt lgkmcnt(0)
	v_readfirstlane_b32 s20, v10
	v_readfirstlane_b32 s21, v11
	s_nop 1
	v_lshl_add_u64 v[30:31], s[20:21], 0, v[12:13]
	global_load_dword v40, v[30:31], off
	v_lshl_add_u64 v[30:31], v[30:31], 0, s[28:29]
	global_load_dword v41, v[30:31], off
	v_lshl_add_u64 v[30:31], v[30:31], 0, s[28:29]
	global_load_dword v42, v[30:31], off
	v_lshl_add_u64 v[30:31], v[30:31], 0, s[28:29]
	global_load_dword v43, v[30:31], off
	v_lshl_add_u64 v[30:31], v[30:31], 0, s[28:29]
	global_load_dword v44, v[30:31], off
	v_lshl_add_u64 v[30:31], v[30:31], 0, s[28:29]
	global_load_dword v45, v[30:31], off
	v_lshl_add_u64 v[30:31], v[30:31], 0, s[28:29]
	global_load_dword v46, v[30:31], off
	v_lshl_add_u64 v[30:31], v[30:31], 0, s[28:29]
	global_load_dword v47, v[30:31], off
	v_lshl_add_u64 v[30:31], v[30:31], 0, s[28:29]
	global_load_dword v48, v[30:31], off
	v_lshl_add_u64 v[30:31], v[30:31], 0, s[28:29]
	global_load_dword v49, v[30:31], off
	v_lshl_add_u64 v[30:31], v[30:31], 0, s[28:29]
	global_load_dword v50, v[30:31], off
	v_lshl_add_u64 v[30:31], v[30:31], 0, s[28:29]
	global_load_dword v51, v[30:31], off
	v_lshl_add_u64 v[30:31], v[30:31], 0, s[28:29]
	global_load_dword v52, v[30:31], off
	v_lshl_add_u64 v[30:31], v[30:31], 0, s[28:29]
	global_load_dword v53, v[30:31], off
	v_lshl_add_u64 v[30:31], v[30:31], 0, s[28:29]
	global_load_dword v54, v[30:31], off
	v_lshl_add_u64 v[30:31], v[30:31], 0, s[28:29]
	global_load_dword v55, v[30:31], off
	s_waitcnt vmcnt(0)
	ds_write_b32 v28, v40
	ds_write_b32 v28, v41 offset:2048
	ds_write_b32 v28, v42 offset:4096
	ds_write_b32 v28, v43 offset:6144
	ds_write_b32 v28, v44 offset:8192
	ds_write_b32 v28, v45 offset:10240
	ds_write_b32 v28, v46 offset:12288
	ds_write_b32 v28, v47 offset:14336
	ds_write_b32 v28, v48 offset:16384
	ds_write_b32 v28, v49 offset:18432
	ds_write_b32 v28, v50 offset:20480
	ds_write_b32 v28, v51 offset:22528
	ds_write_b32 v28, v52 offset:24576
	ds_write_b32 v28, v53 offset:26624
	ds_write_b32 v28, v54 offset:28672
	ds_write_b32 v28, v55 offset:30720

; #define GAS __attribute__((address_space(1)))
; #define LAS __attribute__((address_space(3)))
; __device__ __forceinline__ void hy_conv_item(Frame& F, int l, int c) {
;     ...
;         for (int i = tid; i < 2048; i += NTHR) *(LAS f32x4*)(HS + 4 * i) = *(const GAS f32x4*)(hf + 4 * i);
.LBB0_669:
	v_ashrrev_i32_e32 v3, 31, v2
	v_lshl_add_u64 v[6:7], v[2:3], 2, s[16:17]
	global_load_dwordx4 v[12:15], v[6:7], off
	v_add_co_u32_e32 v6, vcc, 0x2000, v6
	v_addc_co_u32_e32 v7, vcc, 0, v7, vcc
	global_load_dwordx4 v[16:19], v[6:7], off
	v_add_co_u32_e32 v6, vcc, 0x2000, v6
	v_addc_co_u32_e32 v7, vcc, 0, v7, vcc
	global_load_dwordx4 v[20:23], v[6:7], off
	v_add_co_u32_e32 v6, vcc, 0x2000, v6
	v_addc_co_u32_e32 v7, vcc, 0, v7, vcc
	global_load_dwordx4 v[24:27], v[6:7], off
	s_waitcnt vmcnt(0)
	ds_write_b128 v4, v[12:15]
	ds_write_b128 v4, v[16:19] offset:8192
	ds_write_b128 v4, v[20:23] offset:16384
	ds_write_b128 v4, v[24:27] offset:24576

; #define GAS __attribute__((address_space(1)))
; #define LAS __attribute__((address_space(3)))
; __device__ __forceinline__ void hy_conv_item(Frame& F, int l, int c) {
;     ...
;     for (int i = tid; i < BATCH * SEQ / 8; i += NTHR) { const int b = i >> 9, s8 = i & 511, S = s8 >> 3, j8 = s8 & 7;
;         *(LAS v4u*)(Z + (S * 4 + b) * HYC_ZROW + j8 * 16) = *(const GAS v4u*)(zt + (size_t)b * SEQ + s8 * 8); }
.LBB0_697:
	v_ashrrev_i32_e32 v10, 9, v4
	v_ashrrev_i32_e32 v11, 31, v10
	v_lshlrev_b64 v[6:7], 13, v[10:11]
	v_and_b32_e32 v5, 0xff8, v2
	v_lshl_add_u64 v[6:7], s[18:19], 0, v[6:7]
	v_lshlrev_b32_e32 v182, 1, v5
	v_lshl_add_u64 v[6:7], v[6:7], 0, v[182:183]
	global_load_dwordx4 v[12:15], v[6:7], off
	v_lshrrev_b32_e32 v5, 1, v4
	v_and_b32_e32 v5, 0xfc, v5
	v_add_u32_e32 v5, v5, v10
	v_mul_i32_i24_e32 v5, 0x90, v5
	v_and_b32_e32 v10, 0x70, v3
	v_add3_u32 v28, s47, v5, v10
	v_add_u32_e32 v3, 0x2000, v3
	v_add_u32_e32 v2, 0x1000, v2
	v_add_u32_e32 v4, 0x200, v4
	v_ashrrev_i32_e32 v10, 9, v4
	v_ashrrev_i32_e32 v11, 31, v10
	v_lshlrev_b64 v[6:7], 13, v[10:11]
	v_and_b32_e32 v5, 0xff8, v2
	v_lshl_add_u64 v[6:7], s[18:19], 0, v[6:7]
	v_lshlrev_b32_e32 v182, 1, v5
	v_lshl_add_u64 v[6:7], v[6:7], 0, v[182:183]
	global_load_dwordx4 v[16:19], v[6:7], off
	v_lshrrev_b32_e32 v5, 1, v4
	v_and_b32_e32 v5, 0xfc, v5
	v_add_u32_e32 v5, v5, v10
	v_mul_i32_i24_e32 v5, 0x90, v5
	v_and_b32_e32 v10, 0x70, v3
	v_add3_u32 v29, s47, v5, v10
	v_add_u32_e32 v3, 0x2000, v3
	v_add_u32_e32 v2, 0x1000, v2
	v_add_u32_e32 v4, 0x200, v4
	v_ashrrev_i32_e32 v10, 9, v4
	v_ashrrev_i32_e32 v11, 31, v10
	v_lshlrev_b64 v[6:7], 13, v[10:11]
	v_and_b32_e32 v5, 0xff8, v2
	v_lshl_add_u64 v[6:7], s[18:19], 0, v[6:7]
	v_lshlrev_b32_e32 v182, 1, v5
	v_lshl_add_u64 v[6:7], v[6:7], 0, v[182:183]
	global_load_dwordx4 v[20:23], v[6:7], off
	v_lshrrev_b32_e32 v5, 1, v4
	v_and_b32_e32 v5, 0xfc, v5
	v_add_u32_e32 v5, v5, v10
	v_mul_i32_i24_e32 v5, 0x90, v5
	v_and_b32_e32 v10, 0x70, v3
	v_add3_u32 v30, s47, v5, v10
	v_add_u32_e32 v3, 0x2000, v3
	v_add_u32_e32 v2, 0x1000, v2
	v_add_u32_e32 v4, 0x200, v4
	v_ashrrev_i32_e32 v10, 9, v4
	v_ashrrev_i32_e32 v11, 31, v10
	v_lshlrev_b64 v[6:7], 13, v[10:11]
	v_and_b32_e32 v5, 0xff8, v2
	v_lshl_add_u64 v[6:7], s[18:19], 0, v[6:7]
	v_lshlrev_b32_e32 v182, 1, v5
	v_lshl_add_u64 v[6:7], v[6:7], 0, v[182:183]
	global_load_dwordx4 v[24:27], v[6:7], off
	v_lshrrev_b32_e32 v5, 1, v4
	v_and_b32_e32 v5, 0xfc, v5
	v_add_u32_e32 v5, v5, v10
	v_mul_i32_i24_e32 v5, 0x90, v5
	v_and_b32_e32 v10, 0x70, v3
	v_add3_u32 v31, s47, v5, v10
	v_add_u32_e32 v3, 0x2000, v3
	v_add_u32_e32 v2, 0x1000, v2
	v_add_u32_e32 v4, 0x200, v4
	s_waitcnt vmcnt(0)
	ds_write_b128 v28, v[12:15]
	ds_write_b128 v29, v[16:19]
	ds_write_b128 v30, v[20:23]
	ds_write_b128 v31, v[24:27]

; #define GAS __attribute__((address_space(1)))
; #define LAS __attribute__((address_space(3)))
; __device__ __forceinline__ void phase_post_mix(Frame& F, int l) {
;     ...
;     for (int i = F.tid; i < DM * NEXP / 4; i += NTHR) { const int k = i >> 2, part = i & 3, g = k >> 2, slot_ = (g >> 2) + 64 * (g & 3);
;         *(LAS f32x4*)(rws + slot_ * 68 + (k & 3) * 16 + part * 4) = ((const GAS f32x4*)(INP(F, I_ROUTER) + (size_t)l * DM * NEXP))[i]; }
.LBB0_1212:
	v_ashrrev_i32_e32 v6, 6, v5
	v_and_b32_e32 v7, 0xc0, v4
	v_add_u32_e32 v9, v7, v6
	v_mov_b32_e32 v6, s21
	ds_read_b64 v[6:7], v6
	s_waitcnt lgkmcnt(0)
	v_readfirstlane_b32 s6, v6
	v_readfirstlane_b32 s7, v7
	s_nop 1
	v_lshl_add_u64 v[6:7], s[6:7], 0, v[2:3]
	global_load_dwordx4 v[188:191], v[6:7], off
	v_mul_lo_u32 v6, v9, s23
	v_and_b32_e32 v7, 48, v4
	v_and_b32_e32 v9, 12, v4
	v_add_u32_e32 v6, 0, v6
	v_lshlrev_b32_e32 v7, 2, v7
	v_lshlrev_b32_e32 v9, 2, v9
	v_add3_u32 v6, v6, v7, v9
	v_lshl_add_u64 v[2:3], v[2:3], 0, s[28:29]
	v_add_u32_e32 v4, 0x800, v4
	v_mov_b32_e32 v164, v6
	v_add_u32_e32 v6, 0x200, v5
	v_mov_b32_e32 v5, v6
	v_ashrrev_i32_e32 v6, 6, v5
	v_and_b32_e32 v7, 0xc0, v4
	v_add_u32_e32 v9, v7, v6
	v_mov_b32_e32 v6, s21
	ds_read_b64 v[6:7], v6
	s_waitcnt lgkmcnt(0)
	v_readfirstlane_b32 s6, v6
	v_readfirstlane_b32 s7, v7
	s_nop 1
	v_lshl_add_u64 v[6:7], s[6:7], 0, v[2:3]
	global_load_dwordx4 v[192:195], v[6:7], off
	v_mul_lo_u32 v6, v9, s23
	v_and_b32_e32 v7, 48, v4
	v_and_b32_e32 v9, 12, v4
	v_add_u32_e32 v6, 0, v6
	v_lshlrev_b32_e32 v7, 2, v7
	v_lshlrev_b32_e32 v9, 2, v9
	v_add3_u32 v6, v6, v7, v9
	v_lshl_add_u64 v[2:3], v[2:3], 0, s[28:29]
	v_add_u32_e32 v4, 0x800, v4
	v_mov_b32_e32 v165, v6
	v_add_u32_e32 v6, 0x200, v5
	v_mov_b32_e32 v5, v6
	v_ashrrev_i32_e32 v6, 6, v5
	v_and_b32_e32 v7, 0xc0, v4
	v_add_u32_e32 v9, v7, v6
	v_mov_b32_e32 v6, s21
	ds_read_b64 v[6:7], v6
	s_waitcnt lgkmcnt(0)
	v_readfirstlane_b32 s6, v6
	v_readfirstlane_b32 s7, v7
	s_nop 1
	v_lshl_add_u64 v[6:7], s[6:7], 0, v[2:3]
	global_load_dwordx4 v[196:199], v[6:7], off
	v_mul_lo_u32 v6, v9, s23
	v_and_b32_e32 v7, 48, v4
	v_and_b32_e32 v9, 12, v4
	v_add_u32_e32 v6, 0, v6
	v_lshlrev_b32_e32 v7, 2, v7
	v_lshlrev_b32_e32 v9, 2, v9
	v_add3_u32 v6, v6, v7, v9
	v_lshl_add_u64 v[2:3], v[2:3], 0, s[28:29]
	v_add_u32_e32 v4, 0x800, v4
	v_mov_b32_e32 v166, v6
	v_add_u32_e32 v6, 0x200, v5
	v_mov_b32_e32 v5, v6
	v_ashrrev_i32_e32 v6, 6, v5
	v_and_b32_e32 v7, 0xc0, v4
	v_add_u32_e32 v9, v7, v6
	v_mov_b32_e32 v6, s21
	ds_read_b64 v[6:7], v6
	s_waitcnt lgkmcnt(0)
	v_readfirstlane_b32 s6, v6
	v_readfirstlane_b32 s7, v7
	s_nop 1
	v_lshl_add_u64 v[6:7], s[6:7], 0, v[2:3]
	global_load_dwordx4 v[200:203], v[6:7], off
	v_mul_lo_u32 v6, v9, s23
	v_and_b32_e32 v7, 48, v4
	v_and_b32_e32 v9, 12, v4
	v_add_u32_e32 v6, 0, v6
	v_lshlrev_b32_e32 v7, 2, v7
	v_lshlrev_b32_e32 v9, 2, v9
	v_add3_u32 v6, v6, v7, v9
	v_lshl_add_u64 v[2:3], v[2:3], 0, s[28:29]
	v_add_u32_e32 v4, 0x800, v4
	v_mov_b32_e32 v167, v6
	v_add_u32_e32 v6, 0x200, v5
	v_mov_b32_e32 v5, v6
	v_ashrrev_i32_e32 v6, 6, v5
	v_and_b32_e32 v7, 0xc0, v4
	v_add_u32_e32 v9, v7, v6
	v_mov_b32_e32 v6, s21
	ds_read_b64 v[6:7], v6
	s_waitcnt lgkmcnt(0)
	v_readfirstlane_b32 s6, v6
	v_readfirstlane_b32 s7, v7
	s_nop 1
	v_lshl_add_u64 v[6:7], s[6:7], 0, v[2:3]
	global_load_dwordx4 v[204:207], v[6:7], off
	v_mul_lo_u32 v6, v9, s23
	v_and_b32_e32 v7, 48, v4
	v_and_b32_e32 v9, 12, v4
	v_add_u32_e32 v6, 0, v6
	v_lshlrev_b32_e32 v7, 2, v7
	v_lshlrev_b32_e32 v9, 2, v9
	v_add3_u32 v6, v6, v7, v9
	v_lshl_add_u64 v[2:3], v[2:3], 0, s[28:29]
	v_add_u32_e32 v4, 0x800, v4
	v_mov_b32_e32 v168, v6
	v_add_u32_e32 v6, 0x200, v5
	v_mov_b32_e32 v5, v6
	v_ashrrev_i32_e32 v6, 6, v5
	v_and_b32_e32 v7, 0xc0, v4
	v_add_u32_e32 v9, v7, v6
	v_mov_b32_e32 v6, s21
	ds_read_b64 v[6:7], v6
	s_waitcnt lgkmcnt(0)
	v_readfirstlane_b32 s6, v6
	v_readfirstlane_b32 s7, v7
	s_nop 1
	v_lshl_add_u64 v[6:7], s[6:7], 0, v[2:3]
	global_load_dwordx4 v[208:211], v[6:7], off
	v_mul_lo_u32 v6, v9, s23
	v_and_b32_e32 v7, 48, v4
	v_and_b32_e32 v9, 12, v4
	v_add_u32_e32 v6, 0, v6
	v_lshlrev_b32_e32 v7, 2, v7
	v_lshlrev_b32_e32 v9, 2, v9
	v_add3_u32 v6, v6, v7, v9
	v_lshl_add_u64 v[2:3], v[2:3], 0, s[28:29]
	v_add_u32_e32 v4, 0x800, v4
	v_mov_b32_e32 v169, v6
	v_add_u32_e32 v6, 0x200, v5
	v_mov_b32_e32 v5, v6
	v_ashrrev_i32_e32 v6, 6, v5
	v_and_b32_e32 v7, 0xc0, v4
	v_add_u32_e32 v9, v7, v6
	v_mov_b32_e32 v6, s21
	ds_read_b64 v[6:7], v6
	s_waitcnt lgkmcnt(0)
	v_readfirstlane_b32 s6, v6
	v_readfirstlane_b32 s7, v7
	s_nop 1
	v_lshl_add_u64 v[6:7], s[6:7], 0, v[2:3]
	global_load_dwordx4 v[212:215], v[6:7], off
	v_mul_lo_u32 v6, v9, s23
	v_and_b32_e32 v7, 48, v4
	v_and_b32_e32 v9, 12, v4
	v_add_u32_e32 v6, 0, v6
	v_lshlrev_b32_e32 v7, 2, v7
	v_lshlrev_b32_e32 v9, 2, v9
	v_add3_u32 v6, v6, v7, v9
	v_lshl_add_u64 v[2:3], v[2:3], 0, s[28:29]
	v_add_u32_e32 v4, 0x800, v4
	v_mov_b32_e32 v170, v6
	v_add_u32_e32 v6, 0x200, v5
	v_mov_b32_e32 v5, v6
	v_ashrrev_i32_e32 v6, 6, v5
	v_and_b32_e32 v7, 0xc0, v4
	v_add_u32_e32 v9, v7, v6
	v_mov_b32_e32 v6, s21
	ds_read_b64 v[6:7], v6
	s_waitcnt lgkmcnt(0)
	v_readfirstlane_b32 s6, v6
	v_readfirstlane_b32 s7, v7
	s_nop 1
	v_lshl_add_u64 v[6:7], s[6:7], 0, v[2:3]
	global_load_dwordx4 v[216:219], v[6:7], off
	v_mul_lo_u32 v6, v9, s23
	v_and_b32_e32 v7, 48, v4
	v_and_b32_e32 v9, 12, v4
	v_add_u32_e32 v6, 0, v6
	v_lshlrev_b32_e32 v7, 2, v7
	v_lshlrev_b32_e32 v9, 2, v9
	v_add3_u32 v6, v6, v7, v9
	v_lshl_add_u64 v[2:3], v[2:3], 0, s[28:29]
	v_add_u32_e32 v4, 0x800, v4
	v_mov_b32_e32 v171, v6
	v_add_u32_e32 v6, 0x200, v5
	v_mov_b32_e32 v5, v6
	s_waitcnt vmcnt(0)
	ds_write_b128 v164, v[188:191]
	ds_write_b128 v165, v[192:195]
	ds_write_b128 v166, v[196:199]
	ds_write_b128 v167, v[200:203]
	ds_write_b128 v168, v[204:207]
	ds_write_b128 v169, v[208:211]
	ds_write_b128 v170, v[212:215]
	ds_write_b128 v171, v[216:219]

; #define GAS __attribute__((address_space(1)))
; #define LAS __attribute__((address_space(3)))
; __device__ __forceinline__ void phase_post_mix(Frame& F, int l) {
;     ...
;     for (int i = F.tid; i < DM * NEXP / 4; i += NTHR) { const int k = i >> 2, part = i & 3, g = k >> 2, slot_ = (g >> 2) + 64 * (g & 3);
;         *(LAS f32x4*)(rws + slot_ * 68 + (k & 3) * 16 + part * 4) = ((const GAS f32x4*)(INP(F, I_ROUTER) + (size_t)l * DM * NEXP))[i]; }
.LBB0_1241:
	v_ashrrev_i32_e32 v7, 6, v6
	v_and_b32_e32 v8, 0xc0, v3
	v_add_u32_e32 v7, v8, v7
	v_mov_b32_e32 v8, s21
	ds_read_b64 v[8:9], v8
	v_mul_lo_u32 v7, v7, s23
	v_and_b32_e32 v12, 48, v3
	v_and_b32_e32 v13, 12, v3
	v_add_u32_e32 v7, 0, v7
	s_waitcnt lgkmcnt(0)
	v_readfirstlane_b32 s6, v8
	v_readfirstlane_b32 s7, v9
	v_lshlrev_b32_e32 v12, 2, v12
	v_lshlrev_b32_e32 v13, 2, v13
	v_lshl_add_u64 v[8:9], s[6:7], 0, v[4:5]
	global_load_dwordx4 v[188:191], v[8:9], off
	v_add3_u32 v7, v7, v12, v13
	v_lshl_add_u64 v[4:5], v[4:5], 0, s[28:29]
	v_add_u32_e32 v3, 0x800, v3
	v_mov_b32_e32 v164, v7
	v_add_u32_e32 v7, 0x200, v6
	v_mov_b32_e32 v6, v7
	v_ashrrev_i32_e32 v7, 6, v6
	v_and_b32_e32 v8, 0xc0, v3
	v_add_u32_e32 v7, v8, v7
	v_mov_b32_e32 v8, s21
	ds_read_b64 v[8:9], v8
	v_mul_lo_u32 v7, v7, s23
	v_and_b32_e32 v12, 48, v3
	v_and_b32_e32 v13, 12, v3
	v_add_u32_e32 v7, 0, v7
	s_waitcnt lgkmcnt(0)
	v_readfirstlane_b32 s6, v8
	v_readfirstlane_b32 s7, v9
	v_lshlrev_b32_e32 v12, 2, v12
	v_lshlrev_b32_e32 v13, 2, v13
	v_lshl_add_u64 v[8:9], s[6:7], 0, v[4:5]
	global_load_dwordx4 v[192:195], v[8:9], off
	v_add3_u32 v7, v7, v12, v13
	v_lshl_add_u64 v[4:5], v[4:5], 0, s[28:29]
	v_add_u32_e32 v3, 0x800, v3
	v_mov_b32_e32 v165, v7
	v_add_u32_e32 v7, 0x200, v6
	v_mov_b32_e32 v6, v7
	v_ashrrev_i32_e32 v7, 6, v6
	v_and_b32_e32 v8, 0xc0, v3
	v_add_u32_e32 v7, v8, v7
	v_mov_b32_e32 v8, s21
	ds_read_b64 v[8:9], v8
	v_mul_lo_u32 v7, v7, s23
	v_and_b32_e32 v12, 48, v3
	v_and_b32_e32 v13, 12, v3
	v_add_u32_e32 v7, 0, v7
	s_waitcnt lgkmcnt(0)
	v_readfirstlane_b32 s6, v8
	v_readfirstlane_b32 s7, v9
	v_lshlrev_b32_e32 v12, 2, v12
	v_lshlrev_b32_e32 v13, 2, v13
	v_lshl_add_u64 v[8:9], s[6:7], 0, v[4:5]
	global_load_dwordx4 v[196:199], v[8:9], off
	v_add3_u32 v7, v7, v12, v13
	v_lshl_add_u64 v[4:5], v[4:5], 0, s[28:29]
	v_add_u32_e32 v3, 0x800, v3
	v_mov_b32_e32 v166, v7
	v_add_u32_e32 v7, 0x200, v6
	v_mov_b32_e32 v6, v7
	v_ashrrev_i32_e32 v7, 6, v6
	v_and_b32_e32 v8, 0xc0, v3
	v_add_u32_e32 v7, v8, v7
	v_mov_b32_e32 v8, s21
	ds_read_b64 v[8:9], v8
	v_mul_lo_u32 v7, v7, s23
	v_and_b32_e32 v12, 48, v3
	v_and_b32_e32 v13, 12, v3
	v_add_u32_e32 v7, 0, v7
	s_waitcnt lgkmcnt(0)
	v_readfirstlane_b32 s6, v8
	v_readfirstlane_b32 s7, v9
	v_lshlrev_b32_e32 v12, 2, v12
	v_lshlrev_b32_e32 v13, 2, v13
	v_lshl_add_u64 v[8:9], s[6:7], 0, v[4:5]
	global_load_dwordx4 v[200:203], v[8:9], off
	v_add3_u32 v7, v7, v12, v13
	v_lshl_add_u64 v[4:5], v[4:5], 0, s[28:29]
	v_add_u32_e32 v3, 0x800, v3
	v_mov_b32_e32 v167, v7
	v_add_u32_e32 v7, 0x200, v6
	v_mov_b32_e32 v6, v7
	v_ashrrev_i32_e32 v7, 6, v6
	v_and_b32_e32 v8, 0xc0, v3
	v_add_u32_e32 v7, v8, v7
	v_mov_b32_e32 v8, s21
	ds_read_b64 v[8:9], v8
	v_mul_lo_u32 v7, v7, s23
	v_and_b32_e32 v12, 48, v3
	v_and_b32_e32 v13, 12, v3
	v_add_u32_e32 v7, 0, v7
	s_waitcnt lgkmcnt(0)
	v_readfirstlane_b32 s6, v8
	v_readfirstlane_b32 s7, v9
	v_lshlrev_b32_e32 v12, 2, v12
	v_lshlrev_b32_e32 v13, 2, v13
	v_lshl_add_u64 v[8:9], s[6:7], 0, v[4:5]
	global_load_dwordx4 v[204:207], v[8:9], off
	v_add3_u32 v7, v7, v12, v13
	v_lshl_add_u64 v[4:5], v[4:5], 0, s[28:29]
	v_add_u32_e32 v3, 0x800, v3
	v_mov_b32_e32 v168, v7
	v_add_u32_e32 v7, 0x200, v6
	v_mov_b32_e32 v6, v7
	v_ashrrev_i32_e32 v7, 6, v6
	v_and_b32_e32 v8, 0xc0, v3
	v_add_u32_e32 v7, v8, v7
	v_mov_b32_e32 v8, s21
	ds_read_b64 v[8:9], v8
	v_mul_lo_u32 v7, v7, s23
	v_and_b32_e32 v12, 48, v3
	v_and_b32_e32 v13, 12, v3
	v_add_u32_e32 v7, 0, v7
	s_waitcnt lgkmcnt(0)
	v_readfirstlane_b32 s6, v8
	v_readfirstlane_b32 s7, v9
	v_lshlrev_b32_e32 v12, 2, v12
	v_lshlrev_b32_e32 v13, 2, v13
	v_lshl_add_u64 v[8:9], s[6:7], 0, v[4:5]
	global_load_dwordx4 v[208:211], v[8:9], off
	v_add3_u32 v7, v7, v12, v13
	v_lshl_add_u64 v[4:5], v[4:5], 0, s[28:29]
	v_add_u32_e32 v3, 0x800, v3
	v_mov_b32_e32 v169, v7
	v_add_u32_e32 v7, 0x200, v6
	v_mov_b32_e32 v6, v7
	v_ashrrev_i32_e32 v7, 6, v6
	v_and_b32_e32 v8, 0xc0, v3
	v_add_u32_e32 v7, v8, v7
	v_mov_b32_e32 v8, s21
	ds_read_b64 v[8:9], v8
	v_mul_lo_u32 v7, v7, s23
	v_and_b32_e32 v12, 48, v3
	v_and_b32_e32 v13, 12, v3
	v_add_u32_e32 v7, 0, v7
	s_waitcnt lgkmcnt(0)
	v_readfirstlane_b32 s6, v8
	v_readfirstlane_b32 s7, v9
	v_lshlrev_b32_e32 v12, 2, v12
	v_lshlrev_b32_e32 v13, 2, v13
	v_lshl_add_u64 v[8:9], s[6:7], 0, v[4:5]
	global_load_dwordx4 v[212:215], v[8:9], off
	v_add3_u32 v7, v7, v12, v13
	v_lshl_add_u64 v[4:5], v[4:5], 0, s[28:29]
	v_add_u32_e32 v3, 0x800, v3
	v_mov_b32_e32 v170, v7
	v_add_u32_e32 v7, 0x200, v6
	v_mov_b32_e32 v6, v7
	v_ashrrev_i32_e32 v7, 6, v6
	v_and_b32_e32 v8, 0xc0, v3
	v_add_u32_e32 v7, v8, v7
	v_mov_b32_e32 v8, s21
	ds_read_b64 v[8:9], v8
	v_mul_lo_u32 v7, v7, s23
	v_and_b32_e32 v12, 48, v3
	v_and_b32_e32 v13, 12, v3
	v_add_u32_e32 v7, 0, v7
	s_waitcnt lgkmcnt(0)
	v_readfirstlane_b32 s6, v8
	v_readfirstlane_b32 s7, v9
	v_lshlrev_b32_e32 v12, 2, v12
	v_lshlrev_b32_e32 v13, 2, v13
	v_lshl_add_u64 v[8:9], s[6:7], 0, v[4:5]
	global_load_dwordx4 v[216:219], v[8:9], off
	v_add3_u32 v7, v7, v12, v13
	v_lshl_add_u64 v[4:5], v[4:5], 0, s[28:29]
	v_add_u32_e32 v3, 0x800, v3
	v_mov_b32_e32 v171, v7
	v_add_u32_e32 v7, 0x200, v6
	v_mov_b32_e32 v6, v7
	s_waitcnt vmcnt(0)
	ds_write_b128 v164, v[188:191]
	ds_write_b128 v165, v[192:195]
	ds_write_b128 v166, v[196:199]
	ds_write_b128 v167, v[200:203]
	ds_write_b128 v168, v[204:207]
	ds_write_b128 v169, v[208:211]
	ds_write_b128 v170, v[212:215]
	ds_write_b128 v171, v[216:219]
